# speedup vs baseline: 1.0079x; 1.0018x over previous
_Z11edge_kernelPKfPK15HIP_vector_typeIjLj4EES0_S0_S4_PfS5_:
	s_cmp_lt_u32 s2, 256
	s_cbranch_scc1 .Ledge_go
	s_cmp_ge_u32 s2, 512
	s_cbranch_scc1 .Ledge_go
	s_sleep 32
.Ledge_go:
	s_load_dwordx8 s[64:71], s[0:1], 0x0
	s_load_dwordx4 s[72:75], s[0:1], 0x20
	s_load_dwordx2 s[76:77], s[0:1], 0x30
	s_waitcnt lgkmcnt(0)
	s_mov_b64 s[4:5], s[72:73]
	v_lshrrev_b32_e32 v192, 6, v0
	s_and_b32 s14, s2, 1
	s_lshr_b32 s3, s2, 6
	s_and_b32 s3, s3, 0x3fffff8
	v_lshl_or_b32 v1, s14, 2, v192
	v_or_b32_e32 v1, s3, v1
	v_lshlrev_b32_e32 v176, 4, v1
	v_mov_b32_e32 v177, 0
	v_and_b32_e32 v191, 63, v0
	v_lshlrev_b64 v[2:3], 10, v[176:177]
	s_waitcnt lgkmcnt(0)
	v_lshl_add_u64 v[2:3], s[4:5], 0, v[2:3]
	v_lshlrev_b32_e32 v176, 4, v191
	v_lshl_add_u64 v[184:185], v[2:3], 0, v[176:177]
	global_load_dwordx4 v[2:5], v[184:185], off
	s_mov_b64 s[4:5], 0x400
	v_lshl_add_u64 v[6:7], v[184:185], 0, s[4:5]
	global_load_dwordx4 v[170:173], v[6:7], off
	s_mov_b64 s[4:5], 0x800
	v_lshl_add_u64 v[6:7], v[184:185], 0, s[4:5]
	global_load_dwordx4 v[166:169], v[6:7], off
	s_mov_b64 s[4:5], 0xc00
	v_lshl_add_u64 v[6:7], v[184:185], 0, s[4:5]
	global_load_dwordx4 v[162:165], v[6:7], off
	s_mov_b64 s[4:5], 0x1000
	v_lshl_add_u64 v[6:7], v[184:185], 0, s[4:5]
	global_load_dwordx4 v[158:161], v[6:7], off
	s_mov_b64 s[4:5], 0x1400
	v_lshl_add_u64 v[6:7], v[184:185], 0, s[4:5]
	global_load_dwordx4 v[154:157], v[6:7], off
	s_mov_b64 s[4:5], 0x1800
	v_lshl_add_u64 v[6:7], v[184:185], 0, s[4:5]
	global_load_dwordx4 v[150:153], v[6:7], off
	s_mov_b64 s[4:5], 0x1c00
	v_lshl_add_u64 v[6:7], v[184:185], 0, s[4:5]
	global_load_dwordx4 v[146:149], v[6:7], off
	s_mov_b64 s[4:5], 0x2000
	v_lshl_add_u64 v[6:7], v[184:185], 0, s[4:5]
	global_load_dwordx4 v[110:113], v[6:7], off
	s_mov_b64 s[4:5], 0x2400
	v_lshl_add_u64 v[6:7], v[184:185], 0, s[4:5]
	global_load_dwordx4 v[90:93], v[6:7], off
	s_mov_b64 s[4:5], 0x2800
	v_lshl_add_u64 v[6:7], v[184:185], 0, s[4:5]
	global_load_dwordx4 v[86:89], v[6:7], off
	s_mov_b64 s[4:5], 0x2c00
	v_lshl_add_u64 v[6:7], v[184:185], 0, s[4:5]
	global_load_dwordx4 v[82:85], v[6:7], off
	v_cmp_lt_u32_e32 vcc, 63, v0
	s_and_saveexec_b64 s[4:5], vcc
	s_xor_b64 s[4:5], exec, s[4:5]
	s_cbranch_execz .LBB1_10
	s_mov_b64 s[6:7], s[68:69]
	v_cmp_lt_i32_e32 vcc, 1, v192
	s_and_saveexec_b64 s[8:9], vcc
	s_xor_b64 s[8:9], exec, s[8:9]
	s_cbranch_execz .LBB1_5
	v_cmp_eq_u32_e32 vcc, 2, v192
	s_and_saveexec_b64 s[10:11], vcc
	s_cbranch_execz .LBB1_4
	s_mov_b64 s[12:13], src_shared_base
	v_mov_b32_e32 v177, 0
	s_mov_b32 s12, 0xe800
	s_waitcnt lgkmcnt(0)
	v_lshl_add_u64 v[6:7], s[6:7], 0, v[176:177]
	s_mov_b64 s[16:17], 0x400
	s_cmp_lg_u64 s[12:13], 0
	v_lshl_add_u64 v[6:7], v[6:7], 0, s[16:17]
	s_cselect_b32 m0, 0xe800, -1
	s_nop 0
	global_load_lds_dwordx4 v[6:7], off
